# speedup vs baseline: 1.0085x; 1.0085x over previous
.Lstag_done_p3:
	s_mov_b32 s66, s2
	s_load_dwordx2 s[64:65], s[0:1], 0x0
	v_lshrrev_b32_e32 v162, 6, v0
	v_bfe_u32 v163, v0, 2, 4
	v_lshl_add_u32 v162, v162, 7, v163
	v_lshlrev_b32_e32 v163, 4, v0
	v_and_b32_e32 v163, 48, v163
	v_lshl_add_u32 v162, v162, 9, v163
	s_load_dwordx8 s[4:11], s[0:1], 0x0
	s_load_dwordx2 s[16:17], s[0:1], 0x20
	s_load_dwordx4 s[12:15], s[0:1], 0x30
	s_ashr_i32 s0, s2, 3
	s_mul_hi_i32 s18, s0, 0x55555556
	s_lshr_b32 s19, s18, 31
	s_add_i32 s21, s18, s19
	s_mul_i32 s18, s21, 0x3fffffd
	s_bfe_u32 s1, s2, 0x20001
	s_add_i32 s18, s18, s0
	s_lshl_b32 s2, s2, 5
	s_lshl_b32 s0, s18, 6
	s_and_b32 s2, s2, 32
	s_or_b32 s0, s0, s2
	s_lshl_b32 s2, s21, 1
	s_and_b32 s19, s2, -16
	s_lshl_b32 s2, s21, 4
	s_and_b32 s20, s2, 0x70
	s_mul_i32 s2, s1, 0xc0
	s_add_i32 s18, s0, s2
	s_mov_b32 s3, 0
	v_mov_b32_e32 v50, 0
	v_lshrrev_b32_e32 v142, 6, v0
	v_bfe_u32 v45, v0, 2, 4
	v_lshlrev_b32_e32 v1, 4, v0
	v_and_b32_e32 v34, 48, v1
	v_lshl_add_u32 v1, v142, 7, v45
	v_lshl_add_u32 v1, v1, 9, v34
	s_lshl_b32 s22, s18, 7
	s_add_i32 s22, s22, s19
	s_lshl_b32 s22, s22, 9
	s_lshl_b32 s2, s20, 2
	s_add_i32 s22, s22, s2
	s_waitcnt lgkmcnt(0)
	s_add_u32 s24, s4, s22
	s_addc_u32 s25, s5, 0
	s_add_u32 s26, s24, 0x40000
	s_addc_u32 s27, s25, 0
	s_add_u32 s28, s26, 0x40000
	s_addc_u32 s29, s27, 0
	s_add_u32 s30, s28, 0x40000
	s_addc_u32 s31, s29, 0
	s_add_u32 s32, s30, 0x40000
	s_addc_u32 s33, s31, 0
	s_add_u32 s34, s32, 0x40000
	s_addc_u32 s35, s33, 0
	s_add_u32 s36, s34, 0x40000
	s_addc_u32 s37, s35, 0
	s_add_u32 s38, s36, 0x40000
	s_addc_u32 s39, s37, 0
	global_load_dwordx4 v[2:5], v1, s[38:39]
	global_load_dwordx4 v[6:9], v1, s[36:37]
	global_load_dwordx4 v[10:13], v1, s[34:35]
	global_load_dwordx4 v[14:17], v1, s[32:33]
	global_load_dwordx4 v[18:21], v1, s[30:31]
	global_load_dwordx4 v[22:25], v1, s[28:29]
	v_and_b32_e32 v35, 31, v0
	global_load_dwordx4 v[26:29], v1, s[26:27]
	global_load_dwordx4 v[30:33], v1, s[24:25]
	v_or_b32_e32 v36, s0, v35
	v_ashrrev_i32_e32 v37, 31, v36
	v_lshlrev_b64 v[38:39], 2, v[36:37]
	v_lshlrev_b32_e32 v89, 1, v142
	v_and_b32_e32 v1, 3, v0
	v_lshrrev_b32_e32 v37, 1, v0
	v_lshl_add_u64 v[40:41], s[16:17], 0, v[38:39]
	v_and_or_b32 v144, v37, 12, v1
	v_or_b32_e32 v1, s20, v89
	global_load_dword v94, v[40:41], off
	v_bfe_u32 v143, v0, 2, 1
	v_lshlrev_b32_e32 v40, 1, v35
	v_mov_b32_e32 v41, v50
	v_or_b32_e32 v37, 8, v1
	v_bfe_u32 v95, v0, 5, 1
	s_lshl_b32 s4, s1, 16
	v_lshl_add_u64 v[86:87], s[12:13], 0, v[40:41]
	v_or_b32_e32 v51, s19, v144
	v_or_b32_e32 v40, v37, v143
	v_lshlrev_b32_e32 v82, 4, v95
	v_mov_b32_e32 v83, v50
	s_ashr_i32 s5, s0, 5
	s_or_b32 s0, s4, 0x4000
	v_lshl_add_u32 v42, v40, 7, v51
	v_lshl_add_u64 v[84:85], s[6:7], 0, v[82:83]
	s_or_b32 s2, s4, 0xc000
	s_mul_i32 s7, s1, 24
	v_add_u32_e32 v40, s0, v42
	s_or_b32 s1, s7, 6
	v_ashrrev_i32_e32 v41, 31, v40
	v_add_u32_e32 v42, s2, v42
	s_add_i32 s6, s5, 12
	s_ashr_i32 s12, s21, 3
	s_add_i32 s13, s1, s5
	v_lshlrev_b64 v[40:41], 5, v[40:41]
	v_ashrrev_i32_e32 v43, 31, v42
	v_or_b32_e32 v37, v37, v95
	s_lshl_b32 s13, s13, 10
	s_add_i32 s1, s1, s6
	v_lshl_add_u64 v[40:41], v[84:85], 0, v[40:41]
	v_lshlrev_b64 v[42:43], 5, v[42:43]
	v_lshl_add_u32 v37, v37, 3, s12
	s_lshl_b32 s1, s1, 10
	v_lshl_add_u64 v[42:43], v[84:85], 0, v[42:43]
	global_load_dwordx4 v[58:61], v[40:41], off
	global_load_dwordx4 v[62:65], v[42:43], off
	v_add_u32_e32 v40, s13, v37
	v_ashrrev_i32_e32 v41, 31, v40
	v_add_u32_e32 v42, s1, v37
	v_lshlrev_b64 v[40:41], 6, v[40:41]
	v_ashrrev_i32_e32 v43, 31, v42
	v_lshl_or_b32 v88, v36, 1, v95
	v_lshl_add_u64 v[40:41], v[86:87], 0, v[40:41]
	v_lshlrev_b64 v[42:43], 6, v[42:43]
	v_add_u32_e32 v36, 0x180, v88
	v_lshl_add_u64 v[42:43], v[86:87], 0, v[42:43]
	global_load_ushort v145, v[40:41], off
	global_load_ushort v146, v[42:43], off
	v_ashrrev_i32_e32 v37, 31, v36
	v_add_u32_e32 v40, 0x480, v88
	v_lshl_add_u64 v[36:37], v[36:37], 4, s[8:9]
	v_ashrrev_i32_e32 v41, 31, v40
	v_lshl_add_u64 v[40:41], v[40:41], 4, s[8:9]
	global_load_dwordx4 v[66:69], v[36:37], off
	global_load_dwordx4 v[70:73], v[40:41], off
	v_or_b32_e32 v36, v1, v95
	v_lshl_add_u64 v[90:91], s[10:11], 0, v[38:39]
	v_lshl_add_u32 v38, v36, 3, s12
	v_add_u32_e32 v36, s1, v38
	v_ashrrev_i32_e32 v37, 31, v36
	v_add_u32_e32 v38, s13, v38
	v_lshlrev_b64 v[36:37], 6, v[36:37]
	v_ashrrev_i32_e32 v39, 31, v38
	v_or_b32_e32 v1, v1, v143
	v_lshl_add_u64 v[36:37], v[86:87], 0, v[36:37]
	v_lshlrev_b64 v[38:39], 6, v[38:39]
	v_lshl_add_u32 v1, v1, 7, v51
	global_load_dword v92, v[90:91], off offset:2304
	global_load_dword v96, v[90:91], off offset:768
	v_lshl_add_u64 v[38:39], v[86:87], 0, v[38:39]
	global_load_ushort v150, v[36:37], off
	global_load_ushort v151, v[38:39], off
	v_add_u32_e32 v36, s2, v1
	v_ashrrev_i32_e32 v37, 31, v36
	v_add_u32_e32 v38, s0, v1
	v_lshlrev_b64 v[36:37], 5, v[36:37]
	v_ashrrev_i32_e32 v39, 31, v38
	v_lshl_add_u64 v[36:37], v[84:85], 0, v[36:37]
	v_lshlrev_b64 v[38:39], 5, v[38:39]
	v_lshl_add_u64 v[38:39], v[84:85], 0, v[38:39]
	global_load_dwordx4 v[74:77], v[36:37], off
	global_load_dwordx4 v[78:81], v[38:39], off
	v_and_b32_e32 v1, 63, v0
	v_cmp_gt_u32_e32 vcc, 32, v1
	v_bfrev_b32_e32 v1, 60
	v_mul_u32_u24_e32 v83, 0x210, v35
	v_mov_b32_e32 v36, 0x3c00
	v_cndmask_b32_e64 v56, v1, 0, vcc
	v_mul_u32_u24_e32 v1, 0x410, v35
	v_lshl_or_b32 v35, v95, 1, v83
	v_cndmask_b32_e64 v53, v36, 0, vcc
	v_add_u32_e32 v148, 0x8200, v35
	v_mul_u32_u24_e32 v35, 0x410, v142
	v_lshlrev_b32_e32 v36, 6, v45
	v_add3_u32 v34, v35, v36, v34
	s_waitcnt vmcnt(13)
	ds_write_b128 v34, v[30:33]
	ds_write_b128 v34, v[26:29] offset:4160
	ds_write_b128 v34, v[22:25] offset:8320
	ds_write_b128 v34, v[18:21] offset:12480
	ds_write_b128 v34, v[14:17] offset:16640
	ds_write_b128 v34, v[10:13] offset:20800
	ds_write_b128 v34, v[6:9] offset:24960
	ds_write_b128 v34, v[2:5] offset:29120
	s_waitcnt lgkmcnt(0)
	s_barrier
	v_mov_b32_e32 v51, v50
	v_mov_b32_e32 v52, v50
	v_mov_b32_e32 v54, v50
	v_mov_b32_e32 v55, v50
	v_mov_b32_e32 v57, v50
	v_lshl_or_b32 v147, v95, 2, v1
	s_mov_b64 s[0:1], -1
	s_mov_b32 s10, 0x7f61b1e6
	s_mov_b32 s11, 0x42800000
	s_waitcnt vmcnt(5)
	v_mov_b32_e32 v93, v92
	s_waitcnt vmcnt(4)
	v_mov_b32_e32 v97, v96
	s_branch .LBB3_3

.LBB3_10:
	v_add_u32_e32 v6, s19, v89
	v_add_u32_e32 v8, 8, v6
	v_or_b32_e32 v7, s20, v144
	v_or_b32_e32 v2, v8, v143
	v_lshl_or_b32 v4, v2, 7, v7
	s_or_b32 s0, s4, 0x8000
	v_add_u32_e32 v2, s4, v4
	v_ashrrev_i32_e32 v3, 31, v2
	v_add_u32_e32 v4, s0, v4
	v_lshlrev_b64 v[2:3], 5, v[2:3]
	v_ashrrev_i32_e32 v5, 31, v4
	v_lshl_add_u64 v[2:3], v[84:85], 0, v[2:3]
	v_lshlrev_b64 v[4:5], 5, v[4:5]
	s_lshr_b32 s1, s20, 4
	s_add_i32 s2, s7, s5
	s_add_i32 s7, s7, s6
	v_lshl_add_u64 v[4:5], v[84:85], 0, v[4:5]
	global_load_dwordx4 v[58:61], v[2:3], off
	global_load_dwordx4 v[62:65], v[4:5], off
	v_or_b32_e32 v2, v8, v95
	s_lshl_b32 s2, s2, 10
	s_lshl_b32 s3, s7, 10
	v_lshl_or_b32 v4, v2, 3, s1
	v_add_u32_e32 v2, s2, v4
	v_add_u32_e32 v4, s3, v4
	v_ashrrev_i32_e32 v3, 31, v2
	v_ashrrev_i32_e32 v5, 31, v4
	v_lshlrev_b64 v[2:3], 6, v[2:3]
	v_lshlrev_b64 v[4:5], 6, v[4:5]
	v_lshl_add_u64 v[2:3], v[86:87], 0, v[2:3]
	v_lshl_add_u64 v[4:5], v[86:87], 0, v[4:5]
	global_load_ushort v132, v[2:3], off
	global_load_ushort v133, v[4:5], off
	v_ashrrev_i32_e32 v89, 31, v88
	v_add_u32_e32 v4, 0x300, v88
	v_lshl_add_u64 v[2:3], v[88:89], 4, s[8:9]
	v_ashrrev_i32_e32 v5, 31, v4
	v_lshl_add_u64 v[4:5], v[4:5], 4, s[8:9]
	global_load_dwordx4 v[66:69], v[2:3], off
	global_load_dwordx4 v[70:73], v[4:5], off
	global_load_dword v96, v[90:91], off
	global_load_dword v98, v[90:91], off offset:1536
	v_or_b32_e32 v2, v6, v95
	v_lshl_or_b32 v4, v2, 3, s1
	v_add_u32_e32 v2, s3, v4
	v_ashrrev_i32_e32 v3, 31, v2
	v_add_u32_e32 v4, s2, v4
	v_lshlrev_b64 v[2:3], 6, v[2:3]
	v_ashrrev_i32_e32 v5, 31, v4
	v_lshl_add_u64 v[2:3], v[86:87], 0, v[2:3]
	v_lshlrev_b64 v[4:5], 6, v[4:5]
	v_lshl_add_u64 v[4:5], v[86:87], 0, v[4:5]
	global_load_ushort v138, v[2:3], off
	global_load_ushort v139, v[4:5], off
	v_or_b32_e32 v2, v6, v143
	v_lshl_or_b32 v4, v2, 7, v7
	v_add_u32_e32 v2, s0, v4
	v_ashrrev_i32_e32 v3, 31, v2
	v_add_u32_e32 v4, s4, v4
	v_lshlrev_b64 v[2:3], 5, v[2:3]
	v_ashrrev_i32_e32 v5, 31, v4
	v_lshl_add_u64 v[2:3], v[84:85], 0, v[2:3]
	v_lshlrev_b64 v[4:5], 5, v[4:5]
	v_lshl_add_u64 v[4:5], v[84:85], 0, v[4:5]
	global_load_dwordx4 v[90:93], v[2:3], off
	global_load_dwordx4 v[18:21], v[4:5], off
	v_lshl_or_b32 v134, v142, 5, v82
	v_add_u32_e32 v135, 0x8200, v83
	v_mov_b32_e32 v95, v94
	s_mov_b32 s6, 0
	s_mov_b64 s[0:1], -1
	s_mov_b32 s4, 0x7f61b1e6
	s_mov_b32 s5, 0x42800000
	s_waitcnt vmcnt(5)
	v_mov_b32_e32 v97, v96
	s_waitcnt vmcnt(4)
	v_mov_b32_e32 v99, v98
	s_waitcnt vmcnt(0)
	s_branch .LBB3_12
.LBB3_11:
	v_pk_mul_f32 v[4:5], v[98:99], v[34:35]
	s_xor_b64 s[2:3], s[0:1], -1
	v_exp_f32_e32 v6, v5
	v_exp_f32_e32 v7, v4
	v_pk_mul_f32 v[4:5], v[34:35], v[18:19]
	s_nop 0
	v_fma_f32 v5, v48, v6, v5
	v_fmac_f32_e32 v4, v7, v5
	v_pk_fma_f32 v[10:11], v[2:3], v[4:5], v[100:101]
	s_cmp_lg_u32 s6, 0
	s_cbranch_scc1 .Lp3_nobar
	s_waitcnt lgkmcnt(0)
	s_barrier
	s_cmpk_gt_i32 s66, 0x2ff
	s_cbranch_scc1 .Lp3_nopf
	s_add_i32 s43, s66, 0x300
	s_ashr_i32 s60, s43, 3
	s_mul_hi_i32 s61, s60, 0x55555556
	s_lshr_b32 s62, s61, 31
	s_add_i32 s61, s61, s62
	s_mul_i32 s62, s61, 0x3fffffd
	s_add_i32 s62, s62, s60
	s_lshl_b32 s62, s62, 6
	s_lshl_b32 s63, s43, 5
	s_and_b32 s63, s63, 32
	s_or_b32 s62, s62, s63
	s_bfe_u32 s63, s43, 0x20001
	s_mul_i32 s63, s63, 0xc0
	s_add_i32 s62, s62, s63
	s_lshl_b32 s62, s62, 7
	s_lshl_b32 s63, s61, 1
	s_and_b32 s63, s63, -16
	s_add_i32 s62, s62, s63
	s_lshl_b32 s62, s62, 9
	s_lshl_b32 s63, s61, 4
	s_and_b32 s63, s63, 0x70
	s_lshl_b32 s63, s63, 2
	s_add_i32 s62, s62, s63
	s_add_u32 s44, s64, s62
	s_addc_u32 s45, s65, 0
	s_add_u32 s46, s44, 0x40000
	s_addc_u32 s47, s45, 0
	s_add_u32 s48, s46, 0x40000
	s_addc_u32 s49, s47, 0
	s_add_u32 s50, s48, 0x40000
	s_addc_u32 s51, s49, 0
	s_add_u32 s52, s50, 0x40000
	s_addc_u32 s53, s51, 0
	s_add_u32 s54, s52, 0x40000
	s_addc_u32 s55, s53, 0
	s_add_u32 s56, s54, 0x40000
	s_addc_u32 s57, s55, 0
	s_add_u32 s58, s56, 0x40000
	s_addc_u32 s59, s57, 0
	global_load_dwordx4 v[164:167], v162, s[44:45]
	global_load_dwordx4 v[164:167], v162, s[46:47]
	global_load_dwordx4 v[164:167], v162, s[48:49]
	global_load_dwordx4 v[164:167], v162, s[50:51]
	global_load_dwordx4 v[164:167], v162, s[52:53]
	global_load_dwordx4 v[164:167], v162, s[54:55]
	global_load_dwordx4 v[164:167], v162, s[56:57]
	global_load_dwordx4 v[164:167], v162, s[58:59]
.Lp3_nopf:
.Lp3_nobar:
	v_lshl_add_u32 v6, v137, 1, v135
	ds_read_b128 v[2:5], v6
	ds_read_b128 v[6:9], v6 offset:16
	s_waitcnt lgkmcnt(1)
	v_cvt_f32_f16_e32 v12, v2
	v_cvt_f32_f16_sdwa v13, v2 dst_sel:DWORD dst_unused:UNUSED_PAD src0_sel:WORD_1
	v_cvt_f32_f16_e32 v2, v3
	v_cvt_f32_f16_sdwa v3, v3 dst_sel:DWORD dst_unused:UNUSED_PAD src0_sel:WORD_1
	v_cvt_f32_f16_e32 v14, v4
	v_pk_add_f32 v[10:11], v[10:11], v[12:13]
	v_cvt_f32_f16_sdwa v15, v4 dst_sel:DWORD dst_unused:UNUSED_PAD src0_sel:WORD_1
	v_pk_add_f32 v[2:3], v[128:129], v[2:3]
	v_cvt_f32_f16_e32 v4, v5
	v_cvt_f32_f16_sdwa v5, v5 dst_sel:DWORD dst_unused:UNUSED_PAD src0_sel:WORD_1
	v_pk_fma_f32 v[10:11], v[94:95], v[86:87], v[10:11]
	v_pk_fma_f32 v[12:13], v[94:95], v[88:89], v[2:3]
	ds_write_b128 v136, v[10:13]
	s_waitcnt lgkmcnt(1)
	v_cvt_f32_f16_e32 v10, v6
	v_cvt_f32_f16_sdwa v11, v6 dst_sel:DWORD dst_unused:UNUSED_PAD src0_sel:WORD_1
	v_cvt_f32_f16_e32 v6, v7
	v_cvt_f32_f16_sdwa v7, v7 dst_sel:DWORD dst_unused:UNUSED_PAD src0_sel:WORD_1
	v_pk_add_f32 v[2:3], v[36:37], v[14:15]
	v_pk_add_f32 v[4:5], v[38:39], v[4:5]
	v_pk_fma_f32 v[2:3], v[94:95], v[82:83], v[2:3]
	v_pk_fma_f32 v[4:5], v[94:95], v[84:85], v[4:5]
	ds_write_b128 v136, v[2:5] offset:16
	v_pk_add_f32 v[4:5], v[42:43], v[6:7]
	v_cvt_f32_f16_e32 v6, v8
	v_cvt_f32_f16_sdwa v7, v8 dst_sel:DWORD dst_unused:UNUSED_PAD src0_sel:WORD_1
	v_cvt_f32_f16_e32 v8, v9
	v_cvt_f32_f16_sdwa v9, v9 dst_sel:DWORD dst_unused:UNUSED_PAD src0_sel:WORD_1
	v_pk_add_f32 v[2:3], v[40:41], v[10:11]
	v_pk_fma_f32 v[4:5], v[94:95], v[80:81], v[4:5]
	v_pk_fma_f32 v[2:3], v[94:95], v[78:79], v[2:3]
	ds_write_b128 v136, v[2:5] offset:32
	v_pk_add_f32 v[2:3], v[44:45], v[6:7]
	v_pk_add_f32 v[4:5], v[46:47], v[8:9]
	v_pk_fma_f32 v[2:3], v[94:95], v[74:75], v[2:3]
	v_pk_fma_f32 v[4:5], v[94:95], v[76:77], v[4:5]
	ds_write_b128 v136, v[2:5] offset:48
	v_mov_b64_e32 v[92:93], v[64:65]
	v_mov_b64_e32 v[18:19], v[58:59]
	s_movk_i32 s6, 0x80
	s_mov_b64 s[0:1], 0
	s_andn2_b64 vcc, exec, s[2:3]
	v_mov_b32_e32 v138, v133
	v_mov_b32_e32 v139, v132
	v_mov_b64_e32 v[90:91], v[62:63]
	v_mov_b64_e32 v[20:21], v[60:61]
	s_cbranch_vccz .LBB3_19
.LBB3_12:
	s_nop 0
	v_mfma_f32_32x32x16_f16 v[2:17], v[18:21], v[66:69], 0
	v_add_u32_e32 v137, s6, v134
	v_lshl_add_u32 v136, v137, 2, v1
	ds_read_b128 v[86:89], v136
	ds_read_b128 v[82:85], v136 offset:16
	ds_read_b128 v[78:81], v136 offset:32
	ds_read_b128 v[74:77], v136 offset:48
	s_nop 5
	v_exp_f32_e32 v22, v2
	v_exp_f32_e32 v23, v3
	v_mfma_f32_32x32x16_f16 v[34:49], v[18:21], v[54:57], 0
	v_exp_f32_e32 v104, v4
	v_exp_f32_e32 v105, v5
	v_pk_add_f32 v[22:23], v[22:23], 1.0 op_sel_hi:[1,0]
	v_exp_f32_e32 v112, v10
	v_log_f32_e32 v100, v22
	v_log_f32_e32 v101, v23
	v_exp_f32_e32 v113, v11
	s_waitcnt lgkmcnt(3)
	s_nop 3
	v_pk_mul_f32 v[102:103], v[86:87], v[34:35]
	v_pk_add_f32 v[34:35], v[104:105], 1.0 op_sel_hi:[1,0]
	v_pk_mul_f32 v[22:23], v[96:97], v[100:101]
	v_log_f32_e32 v34, v34
	v_exp_f32_e32 v106, v22
	v_log_f32_e32 v35, v35
	v_exp_f32_e32 v107, v23
	v_pk_mul_f32 v[110:111], v[102:103], v[100:101]
	v_pk_mul_f32 v[36:37], v[88:89], v[36:37]
	v_fma_mix_f32 v110, v106, v139, v110 op_sel_hi:[0,1,0]
	v_pk_mul_f32 v[104:105], v[96:97], v[34:35]
	v_fmac_f32_e32 v111, v107, v110
	v_exp_f32_e32 v104, v104
	v_exp_f32_e32 v106, v6
	v_exp_f32_e32 v107, v7
	v_pk_mul_f32 v[118:119], v[36:37], v[34:35]
	v_exp_f32_e32 v108, v105
	v_fma_f32 v118, v104, v111, v118
	v_pk_add_f32 v[104:105], v[106:107], 1.0 op_sel_hi:[1,0]
	v_exp_f32_e32 v106, v8
	v_log_f32_e32 v104, v104
	v_log_f32_e32 v105, v105
	v_exp_f32_e32 v107, v9
	v_fmac_f32_e32 v119, v108, v118
	s_waitcnt lgkmcnt(2)
	v_pk_mul_f32 v[38:39], v[82:83], v[38:39]
	v_pk_mul_f32 v[108:109], v[96:97], v[104:105]
	v_pk_add_f32 v[106:107], v[106:107], 1.0 op_sel_hi:[1,0]
	v_exp_f32_e32 v108, v108
	v_exp_f32_e32 v109, v109
	v_log_f32_e32 v106, v106
	v_log_f32_e32 v107, v107
	v_pk_mul_f32 v[120:121], v[38:39], v[104:105]
	v_pk_mul_f32 v[40:41], v[84:85], v[40:41]
	v_fma_f32 v120, v108, v119, v120
	v_fmac_f32_e32 v121, v109, v120
	v_pk_mul_f32 v[108:109], v[96:97], v[106:107]
	v_pk_mul_f32 v[122:123], v[40:41], v[106:107]
	v_exp_f32_e32 v108, v108
	v_exp_f32_e32 v114, v109
	s_waitcnt lgkmcnt(1)
	v_pk_mul_f32 v[42:43], v[78:79], v[42:43]
	v_exp_f32_e32 v116, v14
	v_fma_f32 v122, v108, v121, v122
	v_pk_add_f32 v[108:109], v[112:113], 1.0 op_sel_hi:[1,0]
	v_exp_f32_e32 v112, v12
	v_log_f32_e32 v108, v108
	v_log_f32_e32 v109, v109
	v_exp_f32_e32 v113, v13
	v_fmac_f32_e32 v123, v114, v122
	v_exp_f32_e32 v117, v15
	v_pk_mul_f32 v[114:115], v[96:97], v[108:109]
	v_pk_add_f32 v[112:113], v[112:113], 1.0 op_sel_hi:[1,0]
	v_exp_f32_e32 v114, v114
	v_exp_f32_e32 v115, v115
	v_log_f32_e32 v112, v112
	v_log_f32_e32 v113, v113
	v_pk_mul_f32 v[124:125], v[42:43], v[108:109]
	v_pk_mul_f32 v[44:45], v[80:81], v[44:45]
	v_fma_f32 v124, v114, v123, v124
	v_fmac_f32_e32 v125, v115, v124
	v_pk_mul_f32 v[114:115], v[96:97], v[112:113]
	v_pk_mul_f32 v[126:127], v[44:45], v[112:113]
	v_exp_f32_e32 v114, v114
	v_exp_f32_e32 v128, v115
	s_waitcnt lgkmcnt(0)
	v_pk_mul_f32 v[46:47], v[74:75], v[46:47]
	v_mfma_f32_32x32x16_f16 v[18:33], v[18:21], v[50:53], 0
	v_fma_f32 v126, v114, v125, v126
	v_add_f32_e64 v114, v116, 1.0
	v_add_f32_e64 v115, v117, 1.0
	v_exp_f32_e32 v116, v16
	v_log_f32_e32 v114, v114
	v_log_f32_e32 v115, v115
	v_exp_f32_e32 v117, v17
	v_fmac_f32_e32 v127, v128, v126
	v_pk_mul_f32 v[48:49], v[76:77], v[48:49]
	v_pk_mul_f32 v[128:129], v[96:97], v[114:115]
	v_pk_add_f32 v[116:117], v[116:117], 1.0 op_sel_hi:[1,0]
	v_exp_f32_e32 v130, v128
	v_log_f32_e32 v116, v116
	v_log_f32_e32 v117, v117
	v_exp_f32_e32 v140, v129
	v_pk_mul_f32 v[128:129], v[46:47], v[114:115]
	s_nop 0
	v_fma_f32 v128, v130, v127, v128
	v_pk_mul_f32 v[130:131], v[96:97], v[116:117]
	v_fmac_f32_e32 v129, v140, v128
	v_exp_f32_e32 v141, v130
	v_exp_f32_e32 v142, v131
	v_pk_mul_f32 v[130:131], v[48:49], v[116:117]
	s_nop 0
	v_fma_f32 v130, v141, v129, v130
	v_fmac_f32_e32 v131, v142, v130
	v_cmp_nlt_f32_e64 vcc, |v131|, s4
	s_cbranch_vccz .LBB3_14
	v_cmp_lt_f32_e32 vcc, s5, v2
	v_cvt_f32_f16_e32 v110, v139
	s_nop 0
	v_cndmask_b32_e32 v2, v100, v2, vcc
	v_cmp_lt_f32_e32 vcc, s5, v3
	s_nop 1
	v_cndmask_b32_e32 v3, v101, v3, vcc
	v_pk_mul_f32 v[100:101], v[96:97], v[2:3]
	v_cmp_lt_f32_e32 vcc, s5, v4
	v_exp_f32_e32 v100, v100
	v_exp_f32_e32 v101, v101
	v_cndmask_b32_e32 v4, v34, v4, vcc
	v_cmp_lt_f32_e32 vcc, s5, v5
	v_pk_mul_f32 v[2:3], v[102:103], v[2:3]
	s_nop 0
	v_cndmask_b32_e32 v5, v35, v5, vcc
	v_pk_mul_f32 v[34:35], v[96:97], v[4:5]
	v_fma_f32 v2, v100, v110, v2
	v_exp_f32_e32 v34, v34
	v_fmac_f32_e32 v3, v101, v2
	v_cmp_lt_f32_e32 vcc, s5, v6
	v_pk_mul_f32 v[100:101], v[18:19], v[2:3]
	v_pk_mul_f32 v[4:5], v[36:37], v[4:5]
	v_cndmask_b32_e32 v2, v104, v6, vcc
	v_cmp_lt_f32_e32 vcc, s5, v7
	v_exp_f32_e32 v35, v35
	v_fma_f32 v4, v34, v3, v4
	v_cndmask_b32_e32 v3, v105, v7, vcc
	v_pk_mul_f32 v[6:7], v[96:97], v[2:3]
	v_fmac_f32_e32 v5, v35, v4
	v_exp_f32_e32 v6, v6
	v_exp_f32_e32 v7, v7
	v_cmp_lt_f32_e32 vcc, s5, v8
	v_pk_mul_f32 v[102:103], v[20:21], v[4:5]
	v_pk_mul_f32 v[2:3], v[38:39], v[2:3]
	v_cndmask_b32_e32 v4, v106, v8, vcc
	v_cmp_lt_f32_e32 vcc, s5, v9
	v_fma_f32 v2, v6, v5, v2
	v_fmac_f32_e32 v3, v7, v2
	v_cndmask_b32_e32 v5, v107, v9, vcc
	v_pk_mul_f32 v[6:7], v[96:97], v[4:5]
	v_cmp_lt_f32_e32 vcc, s5, v10
	v_exp_f32_e32 v6, v6
	v_exp_f32_e32 v7, v7
	v_pk_mul_f32 v[104:105], v[22:23], v[2:3]
	v_pk_mul_f32 v[4:5], v[40:41], v[4:5]
	v_cndmask_b32_e32 v2, v108, v10, vcc
	v_cmp_lt_f32_e32 vcc, s5, v11
	v_fma_f32 v4, v6, v3, v4
	v_fmac_f32_e32 v5, v7, v4
	v_cndmask_b32_e32 v3, v109, v11, vcc
	v_pk_mul_f32 v[6:7], v[96:97], v[2:3]
	v_cmp_lt_f32_e32 vcc, s5, v12
	v_exp_f32_e32 v6, v6
	v_exp_f32_e32 v7, v7
	v_pk_mul_f32 v[106:107], v[24:25], v[4:5]
	v_pk_mul_f32 v[2:3], v[42:43], v[2:3]
	v_cndmask_b32_e32 v4, v112, v12, vcc
	v_cmp_lt_f32_e32 vcc, s5, v13
	v_fma_f32 v2, v6, v5, v2
	v_fmac_f32_e32 v3, v7, v2
	v_cndmask_b32_e32 v5, v113, v13, vcc
	v_pk_mul_f32 v[6:7], v[96:97], v[4:5]
	v_cmp_lt_f32_e32 vcc, s5, v14
	v_exp_f32_e32 v6, v6
	v_exp_f32_e32 v7, v7
	v_pk_mul_f32 v[108:109], v[26:27], v[2:3]
	v_pk_mul_f32 v[4:5], v[44:45], v[4:5]
	v_cndmask_b32_e32 v2, v114, v14, vcc
	v_cmp_lt_f32_e32 vcc, s5, v15
	v_fma_f32 v4, v6, v3, v4
	v_fmac_f32_e32 v5, v7, v4
	v_cndmask_b32_e32 v3, v115, v15, vcc
	v_pk_mul_f32 v[6:7], v[96:97], v[2:3]
	v_cmp_lt_f32_e32 vcc, s5, v16
	v_exp_f32_e32 v6, v6
	v_exp_f32_e32 v7, v7
	v_pk_mul_f32 v[110:111], v[28:29], v[4:5]
	v_pk_mul_f32 v[2:3], v[46:47], v[2:3]
	v_cndmask_b32_e32 v4, v116, v16, vcc
	v_cmp_lt_f32_e32 vcc, s5, v17
	v_fma_f32 v2, v6, v5, v2
	v_fmac_f32_e32 v3, v7, v2
	v_cndmask_b32_e32 v5, v117, v17, vcc
	v_pk_mul_f32 v[6:7], v[96:97], v[4:5]
	v_pk_mul_f32 v[4:5], v[48:49], v[4:5]
	v_exp_f32_e32 v6, v6
	v_exp_f32_e32 v7, v7
	v_pk_mul_f32 v[112:113], v[30:31], v[2:3]
	v_fma_f32 v4, v6, v3, v4
	v_fmac_f32_e32 v5, v7, v4
	v_pk_mul_f32 v[114:115], v[32:33], v[4:5]
	s_branch .LBB3_15

	.amdhsa_kernel _Z11scan_kernelILi3ELi1536ELi3EEvPKfPKDF16_S3_S1_S1_PDv2_DF16_S3_Pf
		.amdhsa_group_segment_fixed_size 50176
		.amdhsa_private_segment_fixed_size 0
		.amdhsa_kernarg_size 64
		.amdhsa_user_sgpr_count 2
		.amdhsa_user_sgpr_dispatch_ptr 0
		.amdhsa_user_sgpr_queue_ptr 0
		.amdhsa_user_sgpr_kernarg_segment_ptr 1
		.amdhsa_user_sgpr_dispatch_id 0
		.amdhsa_user_sgpr_kernarg_preload_length 0
		.amdhsa_user_sgpr_kernarg_preload_offset 0
		.amdhsa_user_sgpr_private_segment_size 0
		.amdhsa_uses_dynamic_stack 0
		.amdhsa_enable_private_segment 0
		.amdhsa_system_sgpr_workgroup_id_x 1
		.amdhsa_system_sgpr_workgroup_id_y 0
		.amdhsa_system_sgpr_workgroup_id_z 0
		.amdhsa_system_sgpr_workgroup_info 0
		.amdhsa_system_vgpr_workitem_id 0
		.amdhsa_next_free_vgpr 168
		.amdhsa_next_free_sgpr 96
		.amdhsa_accum_offset 168
		.amdhsa_reserve_vcc 1
		.amdhsa_float_round_mode_32 0
		.amdhsa_float_round_mode_16_64 0
		.amdhsa_float_denorm_mode_32 3
		.amdhsa_float_denorm_mode_16_64 3
		.amdhsa_dx10_clamp 1
		.amdhsa_ieee_mode 1
		.amdhsa_fp16_overflow 0
		.amdhsa_tg_split 0
		.amdhsa_exception_fp_ieee_invalid_op 0
		.amdhsa_exception_fp_denorm_src 0
		.amdhsa_exception_fp_ieee_div_zero 0
		.amdhsa_exception_fp_ieee_overflow 0
		.amdhsa_exception_fp_ieee_underflow 0
		.amdhsa_exception_fp_ieee_inexact 0
		.amdhsa_exception_int_div_zero 0
	.end_amdhsa_kernel

amdhsa.kernels:
  - .agpr_count:     0
    .args:
      - .actual_access:  read_only
        .address_space:  global
        .offset:         0
        .size:           8
        .value_kind:     global_buffer
      - .actual_access:  read_only
        .address_space:  global
        .offset:         8
        .size:           8
        .value_kind:     global_buffer
      - .actual_access:  read_only
        .address_space:  global
        .offset:         16
        .size:           8
        .value_kind:     global_buffer
      - .actual_access:  read_only
        .address_space:  global
        .offset:         24
        .size:           8
        .value_kind:     global_buffer
      - .actual_access:  read_only
        .address_space:  global
        .offset:         32
        .size:           8
        .value_kind:     global_buffer
      - .actual_access:  read_only
        .address_space:  global
        .offset:         40
        .size:           8
        .value_kind:     global_buffer
      - .actual_access:  write_only
        .address_space:  global
        .offset:         48
        .size:           8
        .value_kind:     global_buffer
      - .actual_access:  write_only
        .address_space:  global
        .offset:         56
        .size:           8
        .value_kind:     global_buffer
      - .actual_access:  write_only
        .address_space:  global
        .offset:         64
        .size:           8
        .value_kind:     global_buffer
      - .actual_access:  write_only
        .address_space:  global
        .offset:         72
        .size:           8
        .value_kind:     global_buffer
    .group_segment_fixed_size: 65536
    .kernarg_segment_align: 8
    .kernarg_segment_size: 80
    .language:       OpenCL C
    .language_version:
      - 2
      - 0
    .max_flat_workgroup_size: 256
    .name:           _Z11proj_kernelPKfS0_S0_S0_S0_S0_PDF16_S1_PfS2_
    .private_segment_fixed_size: 0
    .sgpr_count:     22
    .sgpr_spill_count: 0
    .symbol:         _Z11proj_kernelPKfS0_S0_S0_S0_S0_PDF16_S1_PfS2_.kd
    .uniform_work_group_size: 1
    .uses_dynamic_stack: false
    .vgpr_count:     200
    .vgpr_spill_count: 0
    .wavefront_size: 64
  - .agpr_count:     0
    .args:
      - .actual_access:  read_only
        .address_space:  global
        .offset:         0
        .size:           8
        .value_kind:     global_buffer
      - .actual_access:  write_only
        .address_space:  global
        .offset:         8
        .size:           8
        .value_kind:     global_buffer
    .group_segment_fixed_size: 12672
    .kernarg_segment_align: 8
    .kernarg_segment_size: 16
    .language:       OpenCL C
    .language_version:
      - 2
      - 0
    .max_flat_workgroup_size: 1024
    .name:           _Z12carry_kernelPKDv2_DF16_PDF16_
    .private_segment_fixed_size: 0
    .sgpr_count:     16
    .sgpr_spill_count: 0
    .symbol:         _Z12carry_kernelPKDv2_DF16_PDF16_.kd
    .uniform_work_group_size: 1
    .uses_dynamic_stack: false
    .vgpr_count:     90
    .vgpr_spill_count: 0
    .wavefront_size: 64
  - .agpr_count:     0
    .args:
      - .actual_access:  read_only
        .address_space:  global
        .offset:         0
        .size:           8
        .value_kind:     global_buffer
      - .actual_access:  read_only
        .address_space:  global
        .offset:         8
        .size:           8
        .value_kind:     global_buffer
      - .actual_access:  read_only
        .address_space:  global
        .offset:         16
        .size:           8
        .value_kind:     global_buffer
      - .actual_access:  read_only
        .address_space:  global
        .offset:         24
        .size:           8
        .value_kind:     global_buffer
      - .actual_access:  read_only
        .address_space:  global
        .offset:         32
        .size:           8
        .value_kind:     global_buffer
      - .actual_access:  write_only
        .address_space:  global
        .offset:         40
        .size:           8
        .value_kind:     global_buffer
      - .actual_access:  read_only
        .address_space:  global
        .offset:         48
        .size:           8
        .value_kind:     global_buffer
      - .actual_access:  read_only
        .address_space:  global
        .offset:         56
        .size:           8
        .value_kind:     global_buffer
    .group_segment_fixed_size: 33280
    .kernarg_segment_align: 8
    .kernarg_segment_size: 64
    .language:       OpenCL C
    .language_version:
      - 2
      - 0
    .max_flat_workgroup_size: 256
    .name:           _Z11scan_kernelILi1ELi1536ELi4EEvPKfPKDF16_S3_S1_S1_PDv2_DF16_S3_Pf
    .private_segment_fixed_size: 0
    .sgpr_count:     24
    .sgpr_spill_count: 0
    .symbol:         _Z11scan_kernelILi1ELi1536ELi4EEvPKfPKDF16_S3_S1_S1_PDv2_DF16_S3_Pf.kd
    .uniform_work_group_size: 1
    .uses_dynamic_stack: false
    .vgpr_count:     110
    .vgpr_spill_count: 0
    .wavefront_size: 64
  - .agpr_count:     0
    .args:
      - .actual_access:  read_only
        .address_space:  global
        .offset:         0
        .size:           8
        .value_kind:     global_buffer
      - .actual_access:  read_only
        .address_space:  global
        .offset:         8
        .size:           8
        .value_kind:     global_buffer
      - .actual_access:  read_only
        .address_space:  global
        .offset:         16
        .size:           8
        .value_kind:     global_buffer
      - .actual_access:  read_only
        .address_space:  global
        .offset:         24
        .size:           8
        .value_kind:     global_buffer
      - .actual_access:  read_only
        .address_space:  global
        .offset:         32
        .size:           8
        .value_kind:     global_buffer
      - .actual_access:  read_only
        .address_space:  global
        .offset:         40
        .size:           8
        .value_kind:     global_buffer
      - .actual_access:  read_only
        .address_space:  global
        .offset:         48
        .size:           8
        .value_kind:     global_buffer
      - .actual_access:  write_only
        .address_space:  global
        .offset:         56
        .size:           8
        .value_kind:     global_buffer
    .group_segment_fixed_size: 50176
    .kernarg_segment_align: 8
    .kernarg_segment_size: 64
    .language:       OpenCL C
    .language_version:
      - 2
      - 0
    .max_flat_workgroup_size: 256
    .name:           _Z11scan_kernelILi3ELi1536ELi3EEvPKfPKDF16_S3_S1_S1_PDv2_DF16_S3_Pf
    .private_segment_fixed_size: 0
    .sgpr_count:     28
    .sgpr_spill_count: 0
    .symbol:         _Z11scan_kernelILi3ELi1536ELi3EEvPKfPKDF16_S3_S1_S1_PDv2_DF16_S3_Pf.kd
    .uniform_work_group_size: 1
    .uses_dynamic_stack: false
    .vgpr_count:     168
    .vgpr_spill_count: 0
    .wavefront_size: 64
